# P7 (spatial gating): the eight U-operand loads of a unit are issued together before the LayerNorm/transposition work and waited once with a counted vmcnt, instead of eight serialized load-wait round t
# speedup vs baseline: 1.0283x; 1.0283x over previous
.LBB0_1031:
	s_or_b64 exec, exec, s[20:21]
	ds_read_b128 v[0:3], v57 offset:34816
	ds_read_b128 v[4:7], v58
	ds_read_b128 v[68:71], v57 offset:34848
	ds_read_b128 v[72:75], v58 offset:32
	s_ashr_i32 s10, s2, 4
	s_lshl_b32 s2, s38, 8
	s_waitcnt lgkmcnt(2)
	v_mfma_f32_32x32x16_bf16 v[0:15], v[0:3], v[4:7], 0
	s_ashr_i32 s11, s10, 31
	s_add_u32 s2, s30, s2
	s_addc_u32 s14, s31, 0
	s_lshl_b64 s[10:11], s[10:11], 19
	s_add_u32 s10, s2, s10
	v_mov_b32_e32 v33, v21
	s_addc_u32 s11, s14, s11
	s_waitcnt lgkmcnt(0)
	v_mfma_f32_32x32x16_bf16 v[0:15], v[68:71], v[72:75], v[0:15]
	ds_read_b128 v[68:71], v57 offset:34880
	ds_read_b128 v[72:75], v58 offset:64
	ds_read_b128 v[76:79], v57 offset:34912
	ds_read_b128 v[80:83], v58 offset:96
	s_and_b64 vcc, exec, s[8:9]
	s_mov_b32 s2, s23
	s_waitcnt lgkmcnt(2)
	v_mfma_f32_32x32x16_bf16 v[0:15], v[68:71], v[72:75], v[0:15]
	ds_read_b128 v[68:71], v57 offset:34944
	ds_read_b128 v[72:75], v58 offset:128
	s_waitcnt lgkmcnt(2)
	v_mfma_f32_32x32x16_bf16 v[0:15], v[76:79], v[80:83], v[0:15]
	ds_read_b128 v[76:79], v57 offset:34976
	ds_read_b128 v[80:83], v58 offset:160
	s_waitcnt lgkmcnt(2)
	v_mfma_f32_32x32x16_bf16 v[0:15], v[68:71], v[72:75], v[0:15]
	ds_read_b128 v[68:71], v57 offset:35008
	ds_read_b128 v[72:75], v57 offset:35040
	ds_read_b128 v[84:87], v58 offset:192
	ds_read_b128 v[88:91], v58 offset:224
	s_waitcnt lgkmcnt(4)
	v_mfma_f32_32x32x16_bf16 v[0:15], v[76:79], v[80:83], v[0:15]
	v_lshl_add_u64 v[76:77], s[10:11], 0, v[32:33]
	v_lshl_add_u64 v[92:93], v[76:77], 0, v[34:35]
	s_waitcnt lgkmcnt(1)
	v_mfma_f32_32x32x16_bf16 v[0:15], v[68:71], v[84:87], v[0:15]
	s_waitcnt vmcnt(16)
	v_mov_b32_e32 v68, v100
	v_mov_b32_e32 v69, v101
	v_lshlrev_b32_e32 v33, 16, v68
	s_waitcnt lgkmcnt(0)
	v_mfma_f32_32x32x16_bf16 v[0:15], v[72:75], v[88:91], v[0:15]
	v_and_b32_e32 v37, 0xffff0000, v68
	v_lshlrev_b32_e32 v68, 16, v69
	v_and_b32_e32 v69, 0xffff0000, v69
	s_nop 8
	v_add_f32_e32 v0, v20, v0
	v_add_f32_e32 v1, v20, v1
	v_add_f32_e32 v2, v20, v2
	v_add_f32_e32 v3, v20, v3
	v_mul_f32_e32 v0, v0, v33
	v_mul_f32_e32 v1, v1, v37
	v_mul_f32_e32 v2, v2, v68
	v_mul_f32_e32 v3, v3, v69
	v_cvt_pk_bf16_f32 v0, v0, v1
	v_cvt_pk_bf16_f32 v1, v2, v3
	v_mov_b32_e32 v2, v102
	v_mov_b32_e32 v3, v103
	v_add_f32_e32 v4, v20, v4
	v_add_f32_e32 v5, v20, v5
	v_add_f32_e32 v6, v20, v6
	v_add_f32_e32 v7, v20, v7
	global_store_dwordx2 v[92:93], v[0:1], off
	v_mov_b32_e32 v37, v21
	v_lshlrev_b32_e32 v0, 16, v2
	v_and_b32_e32 v1, 0xffff0000, v2
	v_lshlrev_b32_e32 v2, 16, v3
	v_and_b32_e32 v3, 0xffff0000, v3
	v_mul_f32_e32 v0, v4, v0
	v_mul_f32_e32 v1, v5, v1
	v_mul_f32_e32 v2, v6, v2
	v_mul_f32_e32 v3, v7, v3
	v_cvt_pk_bf16_f32 v0, v0, v1
	v_cvt_pk_bf16_f32 v1, v2, v3
	v_mov_b32_e32 v2, v104
	v_mov_b32_e32 v3, v105
	v_add_f32_e32 v4, v20, v8
	v_add_f32_e32 v5, v20, v9
	v_add_f32_e32 v6, v20, v10
	v_add_f32_e32 v7, v20, v11
	global_store_dwordx2 v[92:93], v[0:1], off offset:16
	v_lshlrev_b32_e32 v0, 16, v2
	v_and_b32_e32 v1, 0xffff0000, v2
	v_lshlrev_b32_e32 v2, 16, v3
	v_and_b32_e32 v3, 0xffff0000, v3
	v_mul_f32_e32 v0, v4, v0
	v_mul_f32_e32 v1, v5, v1
	v_mul_f32_e32 v2, v6, v2
	v_mul_f32_e32 v3, v7, v3
	v_cvt_pk_bf16_f32 v0, v0, v1
	v_cvt_pk_bf16_f32 v1, v2, v3
	v_mov_b32_e32 v2, v106
	v_mov_b32_e32 v3, v107
	v_add_f32_e32 v4, v20, v12
	v_add_f32_e32 v5, v20, v13
	v_add_f32_e32 v6, v20, v14
	v_add_f32_e32 v7, v20, v15
	global_store_dwordx2 v[92:93], v[0:1], off offset:32
	v_lshlrev_b32_e32 v0, 16, v2
	v_and_b32_e32 v1, 0xffff0000, v2
	v_lshlrev_b32_e32 v2, 16, v3
	v_and_b32_e32 v3, 0xffff0000, v3
	v_mul_f32_e32 v0, v4, v0
	v_mul_f32_e32 v1, v5, v1
	v_mul_f32_e32 v2, v6, v2
	v_mul_f32_e32 v3, v7, v3
	v_cvt_pk_bf16_f32 v84, v0, v1
	v_cvt_pk_bf16_f32 v85, v2, v3
	ds_read_b128 v[0:3], v57 offset:34816
	ds_read_b128 v[4:7], v58 offset:8704
	ds_read_b128 v[68:71], v57 offset:34848
	ds_read_b128 v[72:75], v58 offset:8736
	s_waitcnt lgkmcnt(2)
	v_mfma_f32_32x32x16_bf16 v[0:15], v[0:3], v[4:7], 0
	s_waitcnt lgkmcnt(0)
	v_mfma_f32_32x32x16_bf16 v[0:15], v[68:71], v[72:75], v[0:15]
	ds_read_b128 v[68:71], v57 offset:34880
	ds_read_b128 v[72:75], v58 offset:8768
	ds_read_b128 v[76:79], v57 offset:34912
	ds_read_b128 v[80:83], v58 offset:8800
	s_waitcnt lgkmcnt(2)
	v_mfma_f32_32x32x16_bf16 v[0:15], v[68:71], v[72:75], v[0:15]
	s_waitcnt lgkmcnt(0)
	v_mfma_f32_32x32x16_bf16 v[0:15], v[76:79], v[80:83], v[0:15]
	ds_read_b128 v[68:71], v57 offset:34944
	ds_read_b128 v[72:75], v58 offset:8832
	ds_read_b128 v[76:79], v57 offset:34976
	ds_read_b128 v[80:83], v58 offset:8864
	s_waitcnt lgkmcnt(2)
	v_mfma_f32_32x32x16_bf16 v[0:15], v[68:71], v[72:75], v[0:15]
	ds_read_b128 v[68:71], v57 offset:35008
	ds_read_b128 v[72:75], v58 offset:8896
	s_waitcnt lgkmcnt(2)
	v_mfma_f32_32x32x16_bf16 v[0:15], v[76:79], v[80:83], v[0:15]
	v_lshl_add_u64 v[76:77], s[10:11], 0, v[36:37]
	v_lshl_add_u64 v[86:87], v[76:77], 0, v[34:35]
	ds_read_b128 v[76:79], v57 offset:35040
	ds_read_b128 v[80:83], v58 offset:8928
	global_store_dwordx2 v[92:93], v[84:85], off offset:48
	s_waitcnt lgkmcnt(2)
	v_mfma_f32_32x32x16_bf16 v[0:15], v[68:71], v[72:75], v[0:15]
	v_mov_b32_e32 v68, v108
	v_mov_b32_e32 v69, v109
	v_lshlrev_b32_e32 v33, 16, v68
	s_waitcnt lgkmcnt(0)
	v_mfma_f32_32x32x16_bf16 v[0:15], v[76:79], v[80:83], v[0:15]
	v_and_b32_e32 v37, 0xffff0000, v68
	v_lshlrev_b32_e32 v68, 16, v69
	v_and_b32_e32 v69, 0xffff0000, v69
	s_nop 8
	v_add_f32_e32 v0, v64, v0
	v_add_f32_e32 v1, v64, v1
	v_add_f32_e32 v2, v64, v2
	v_add_f32_e32 v3, v64, v3
	v_mul_f32_e32 v0, v0, v33
	v_mul_f32_e32 v1, v1, v37
	v_mul_f32_e32 v2, v2, v68
	v_mul_f32_e32 v3, v3, v69
	v_cvt_pk_bf16_f32 v0, v0, v1
	v_cvt_pk_bf16_f32 v1, v2, v3
	v_mov_b32_e32 v2, v110
	v_mov_b32_e32 v3, v111
	v_add_f32_e32 v4, v64, v4
	v_add_f32_e32 v5, v64, v5
	v_add_f32_e32 v6, v64, v6
	v_add_f32_e32 v7, v64, v7
	global_store_dwordx2 v[86:87], v[0:1], off
	v_lshlrev_b32_e32 v0, 16, v2
	v_and_b32_e32 v1, 0xffff0000, v2
	v_lshlrev_b32_e32 v2, 16, v3
	v_and_b32_e32 v3, 0xffff0000, v3
	v_mul_f32_e32 v0, v4, v0
	v_mul_f32_e32 v1, v5, v1
	v_mul_f32_e32 v2, v6, v2
	v_mul_f32_e32 v3, v7, v3
	v_cvt_pk_bf16_f32 v0, v0, v1
	v_cvt_pk_bf16_f32 v1, v2, v3
	v_mov_b32_e32 v2, v112
	v_mov_b32_e32 v3, v113
	v_add_f32_e32 v4, v64, v8
	v_add_f32_e32 v5, v64, v9
	v_add_f32_e32 v6, v64, v10
	v_add_f32_e32 v7, v64, v11
	global_store_dwordx2 v[86:87], v[0:1], off offset:16
	v_lshlrev_b32_e32 v0, 16, v2
	v_and_b32_e32 v1, 0xffff0000, v2
	v_lshlrev_b32_e32 v2, 16, v3
	v_and_b32_e32 v3, 0xffff0000, v3
	v_mul_f32_e32 v0, v4, v0
	v_mul_f32_e32 v1, v5, v1
	v_mul_f32_e32 v2, v6, v2
	v_mul_f32_e32 v3, v7, v3
	v_cvt_pk_bf16_f32 v0, v0, v1
	v_cvt_pk_bf16_f32 v1, v2, v3
	v_mov_b32_e32 v2, v114
	v_mov_b32_e32 v3, v115
	v_add_f32_e32 v4, v64, v12
	v_add_f32_e32 v5, v64, v13
	global_store_dwordx2 v[86:87], v[0:1], off offset:32
	v_add_f32_e32 v6, v64, v14
	v_add_f32_e32 v7, v64, v15
	v_lshlrev_b32_e32 v0, 16, v2
	v_and_b32_e32 v1, 0xffff0000, v2
	v_lshlrev_b32_e32 v2, 16, v3
	v_and_b32_e32 v3, 0xffff0000, v3
	v_mul_f32_e32 v0, v4, v0
	v_mul_f32_e32 v1, v5, v1
	v_mul_f32_e32 v2, v6, v2
	v_mul_f32_e32 v3, v7, v3
	v_cvt_pk_bf16_f32 v0, v0, v1
	v_cvt_pk_bf16_f32 v1, v2, v3
	global_store_dwordx2 v[86:87], v[0:1], off offset:48
	s_waitcnt lgkmcnt(0)
	s_barrier
	s_cbranch_vccnz .LBB0_1041

.LBB0_1037:
	s_ashr_i32 s56, s2, 4
	s_lshl_b32 s58, s38, 8
	s_ashr_i32 s57, s56, 31
	s_add_u32 s58, s30, s58
	s_addc_u32 s59, s31, 0
	s_lshl_b64 s[56:57], s[56:57], 19
	s_add_u32 s56, s58, s56
	s_addc_u32 s57, s59, s57
	v_mov_b32_e32 v117, v21
	v_mov_b32_e32 v116, v32
	v_lshl_add_u64 v[118:119], s[56:57], 0, v[116:117]
	v_lshl_add_u64 v[118:119], v[118:119], 0, v[34:35]
	v_mov_b32_e32 v116, v36
	v_lshl_add_u64 v[120:121], s[56:57], 0, v[116:117]
	v_lshl_add_u64 v[120:121], v[120:121], 0, v[34:35]
	global_load_dwordx2 v[100:101], v[118:119], off
	global_load_dwordx2 v[102:103], v[118:119], off offset:16
	global_load_dwordx2 v[104:105], v[118:119], off offset:32
	global_load_dwordx2 v[106:107], v[118:119], off offset:48
	global_load_dwordx2 v[108:109], v[120:121], off
	global_load_dwordx2 v[110:111], v[120:121], off offset:16
	global_load_dwordx2 v[112:113], v[120:121], off offset:32
	global_load_dwordx2 v[114:115], v[120:121], off offset:48
	s_and_saveexec_b64 s[10:11], s[4:5]
	s_cbranch_execz .LBB0_1039
	v_mul_f32_e32 v0, 0x3a000000, v66
	v_mul_f32_e32 v1, v0, v0
	v_fma_f32 v1, v67, s36, -v1
	v_max_f32_e32 v1, 0, v1
	v_add_f32_e32 v1, 0x358637bd, v1
	v_mul_f32_e32 v2, 0x4f800000, v1
	v_cmp_gt_f32_e32 vcc, s37, v1
	s_nop 1
	v_cndmask_b32_e32 v1, v1, v2, vcc
	v_sqrt_f32_e32 v2, v1
	s_nop 0
	v_add_u32_e32 v3, -1, v2
	v_fma_f32 v5, -v3, v2, v1
	v_add_u32_e32 v4, 1, v2
	v_cmp_ge_f32_e64 s[8:9], 0, v5
	s_nop 1
	v_cndmask_b32_e64 v3, v2, v3, s[8:9]
	v_fma_f32 v2, -v4, v2, v1
	v_cmp_lt_f32_e64 s[8:9], 0, v2
	s_nop 1
	v_cndmask_b32_e64 v2, v3, v4, s[8:9]
	v_mul_f32_e32 v3, 0x37800000, v2
	v_cndmask_b32_e32 v2, v2, v3, vcc
	v_cmp_class_f32_e32 vcc, v1, v54
	s_nop 1
	v_cndmask_b32_e32 v1, v2, v1, vcc
	v_div_scale_f32 v2, s[8:9], v1, v1, 1.0
	v_rcp_f32_e32 v3, v2
	s_nop 0
	v_fma_f32 v4, -v2, v3, 1.0
	v_fmac_f32_e32 v3, v4, v3
	v_div_scale_f32 v4, vcc, 1.0, v1, 1.0
	v_mul_f32_e32 v5, v4, v3
	v_fma_f32 v6, -v2, v5, v4
	v_fmac_f32_e32 v5, v6, v3
	v_fma_f32 v2, -v2, v5, v4
	v_div_fmas_f32 v2, v2, v3, v5
	v_div_fixup_f32 v1, v2, v1, 1.0
	ds_write_b64 v53, v[0:1]
.LBB0_1039:
	s_or_b64 exec, exec, s[10:11]
	s_waitcnt lgkmcnt(0)
	s_barrier
	ds_read_b128 v[0:3], v55
	s_waitcnt vmcnt(11)
	v_lshlrev_b32_e32 v4, 16, v65
	v_and_b32_e32 v6, 0xffff0000, v65
	v_lshlrev_b32_e32 v5, 16, v63
	v_and_b32_e32 v10, 0xffff0000, v60
	s_waitcnt lgkmcnt(0)
	v_sub_f32_e32 v4, v4, v0
	v_sub_f32_e32 v0, v6, v0
	v_mul_f32_e32 v0, v1, v0
	v_mul_f32_e32 v4, v1, v4
	s_waitcnt vmcnt(10)
	v_fma_f32 v1, v39, v0, v41
	v_and_b32_e32 v0, 0xffff0000, v63
	v_sub_f32_e32 v5, v5, v2
	v_sub_f32_e32 v0, v0, v2
	v_fma_f32 v4, v38, v4, v40
	v_mul_f32_e32 v5, v3, v5
	v_mul_f32_e32 v0, v3, v0
	v_fma_f32 v5, v38, v5, v40
	v_fma_f32 v2, v39, v0, v41
	v_cvt_pk_bf16_f32 v0, v4, v5
	v_cvt_pk_bf16_f32 v4, v1, v2
	ds_read_b128 v[6:9], v55 offset:16
	v_lshlrev_b32_e32 v1, 16, v62
	v_and_b32_e32 v5, 0xffff0000, v61
	v_lshlrev_b32_e32 v2, 16, v61
	v_and_b32_e32 v3, 0xffff0000, v62
	s_waitcnt lgkmcnt(0)
	v_sub_f32_e32 v1, v1, v6
	v_sub_f32_e32 v5, v5, v8
	v_mul_f32_e32 v1, v7, v1
	v_sub_f32_e32 v2, v2, v8
	v_sub_f32_e32 v3, v3, v6
	v_mul_f32_e32 v5, v9, v5
	v_fma_f32 v1, v38, v1, v40
	v_mul_f32_e32 v2, v9, v2
	v_mul_f32_e32 v3, v7, v3
	v_fma_f32 v5, v39, v5, v41
	v_fma_f32 v2, v38, v2, v40
	v_fma_f32 v3, v39, v3, v41
	v_cvt_pk_bf16_f32 v1, v1, v2
	v_cvt_pk_bf16_f32 v5, v3, v5
	ds_read_b128 v[6:9], v55 offset:32
	v_lshlrev_b32_e32 v2, 16, v60
	v_lshlrev_b32_e32 v3, 16, v59
	v_and_b32_e32 v12, 0xffff0000, v51
	v_and_b32_e32 v14, 0xffff0000, v44
	s_waitcnt lgkmcnt(0)
	v_sub_f32_e32 v2, v2, v6
	v_sub_f32_e32 v6, v10, v6
	v_mul_f32_e32 v2, v7, v2
	v_mul_f32_e32 v6, v7, v6
	v_and_b32_e32 v7, 0xffff0000, v59
	v_sub_f32_e32 v3, v3, v8
	v_sub_f32_e32 v7, v7, v8
	v_fma_f32 v2, v38, v2, v40
	v_mul_f32_e32 v3, v9, v3
	v_fma_f32 v6, v39, v6, v41
	v_mul_f32_e32 v7, v9, v7
	v_fma_f32 v3, v38, v3, v40
	v_fma_f32 v7, v39, v7, v41
	v_cvt_pk_bf16_f32 v2, v2, v3
	v_cvt_pk_bf16_f32 v6, v6, v7
	ds_read_b128 v[8:11], v55 offset:48
	v_lshlrev_b32_e32 v3, 16, v51
	v_lshlrev_b32_e32 v7, 16, v50
	v_lshlrev_b32_e32 v13, 16, v48
	v_and_b32_e32 v15, 0xffff0000, v52
	s_waitcnt lgkmcnt(0)
	v_sub_f32_e32 v3, v3, v8
	v_sub_f32_e32 v8, v12, v8
	v_mul_f32_e32 v3, v9, v3
	v_mul_f32_e32 v8, v9, v8
	v_and_b32_e32 v9, 0xffff0000, v50
	v_sub_f32_e32 v7, v7, v10
	v_sub_f32_e32 v9, v9, v10
	v_mul_f32_e32 v7, v11, v7
	v_mul_f32_e32 v9, v11, v9
	v_fma_f32 v3, v38, v3, v40
	v_fma_f32 v7, v38, v7, v40
	v_fma_f32 v8, v39, v8, v41
	v_fma_f32 v9, v39, v9, v41
	v_cvt_pk_bf16_f32 v3, v3, v7
	v_cvt_pk_bf16_f32 v7, v8, v9
	ds_read_b128 v[8:11], v55 offset:64
	v_lshlrev_b32_e32 v12, 16, v44
	s_add_i32 s23, s2, s33
	s_cmpk_gt_i32 s23, 0xfff
	s_cselect_b64 s[8:9], -1, 0
	s_waitcnt lgkmcnt(0)
	v_sub_f32_e32 v12, v12, v8
	v_sub_f32_e32 v8, v14, v8
	v_mul_f32_e32 v8, v9, v8
	v_mul_f32_e32 v12, v9, v12
	v_fma_f32 v9, v39, v8, v41
	v_and_b32_e32 v8, 0xffff0000, v48
	v_sub_f32_e32 v13, v13, v10
	v_sub_f32_e32 v8, v8, v10
	v_fma_f32 v12, v38, v12, v40
	v_mul_f32_e32 v13, v11, v13
	v_mul_f32_e32 v8, v11, v8
	v_fma_f32 v13, v38, v13, v40
	v_fma_f32 v10, v39, v8, v41
	v_cvt_pk_bf16_f32 v8, v12, v13
	v_cvt_pk_bf16_f32 v12, v9, v10
	ds_read_b128 v[60:63], v55 offset:80
	v_lshlrev_b32_e32 v9, 16, v43
	v_and_b32_e32 v13, 0xffff0000, v45
	v_lshlrev_b32_e32 v10, 16, v45
	v_and_b32_e32 v11, 0xffff0000, v43
	s_waitcnt lgkmcnt(0)
	v_sub_f32_e32 v9, v9, v60
	v_sub_f32_e32 v13, v13, v62
	v_mul_f32_e32 v9, v61, v9
	v_sub_f32_e32 v10, v10, v62
	v_sub_f32_e32 v11, v11, v60
	v_mul_f32_e32 v13, v63, v13
	v_fma_f32 v9, v38, v9, v40
	v_mul_f32_e32 v10, v63, v10
	v_mul_f32_e32 v11, v61, v11
	v_fma_f32 v13, v39, v13, v41
	v_fma_f32 v10, v38, v10, v40
	v_fma_f32 v11, v39, v11, v41
	v_cvt_pk_bf16_f32 v9, v9, v10
	v_cvt_pk_bf16_f32 v13, v11, v13
	ds_read_b128 v[60:63], v55 offset:96
	v_lshlrev_b32_e32 v10, 16, v27
	v_and_b32_e32 v14, 0xffff0000, v27
	v_lshlrev_b32_e32 v11, 16, v52
	s_cmpk_lt_i32 s23, 0x1000
	s_waitcnt lgkmcnt(0)
	v_sub_f32_e32 v10, v10, v60
	v_sub_f32_e32 v14, v14, v60
	v_mul_f32_e32 v10, v61, v10
	v_sub_f32_e32 v11, v11, v62
	v_mul_f32_e32 v14, v61, v14
	v_sub_f32_e32 v15, v15, v62
	v_fma_f32 v10, v38, v10, v40
	v_mul_f32_e32 v11, v63, v11
	v_fma_f32 v14, v39, v14, v41
	v_mul_f32_e32 v15, v63, v15
	v_fma_f32 v11, v38, v11, v40
	v_fma_f32 v15, v39, v15, v41
	v_cvt_pk_bf16_f32 v10, v10, v11
	v_cvt_pk_bf16_f32 v14, v14, v15
	ds_read_b128 v[60:63], v55 offset:112
	s_cselect_b32 s14, s23, s2
	s_waitcnt vmcnt(9)
	v_lshlrev_b32_e32 v11, 16, v46
	s_waitcnt vmcnt(8)
	v_lshlrev_b32_e32 v15, 16, v47
	s_ashr_i32 s10, s14, 4
	s_waitcnt lgkmcnt(0)
	v_sub_f32_e32 v11, v11, v60
	v_sub_f32_e32 v15, v15, v62
	v_and_b32_e32 v27, 0xffff0000, v46
	v_and_b32_e32 v33, 0xffff0000, v47
	v_mul_f32_e32 v11, v61, v11
	v_mul_f32_e32 v15, v63, v15
	v_sub_f32_e32 v27, v27, v60
	v_sub_f32_e32 v33, v33, v62
	s_ashr_i32 s11, s10, 31
	v_fma_f32 v11, v38, v11, v40
	v_fma_f32 v15, v38, v15, v40
	v_mul_f32_e32 v27, v61, v27
	v_mul_f32_e32 v33, v63, v33
	s_lshl_b64 s[10:11], s[10:11], 7
	v_fma_f32 v27, v39, v27, v41
	v_fma_f32 v33, v39, v33, v41
	v_cvt_pk_bf16_f32 v11, v11, v15
	v_cvt_pk_bf16_f32 v15, v27, v33
	ds_write_b128 v56, v[0:3] offset:34816
	ds_write_b128 v56, v[8:11] offset:34832
	ds_write_b128 v56, v[4:7] offset:35088
	ds_write_b128 v56, v[12:15] offset:35104
	v_lshl_add_u64 v[0:1], s[10:11], 0, v[24:25]
	v_lshlrev_b64 v[0:1], 12, v[0:1]
	s_lshl_b32 s14, s14, 8
	v_lshl_add_u64 v[0:1], s[18:19], 0, v[0:1]
	s_and_b32 s14, s14, 0xf00
	v_lshl_add_u64 v[0:1], v[0:1], 0, s[14:15]
	v_mov_b32_e32 v27, v21
	v_lshl_add_u64 v[0:1], v[0:1], 0, v[26:27]
	v_add_co_u32_e32 v2, vcc, s24, v0
	s_waitcnt lgkmcnt(0)
	s_barrier
	s_nop 0
	v_addc_co_u32_e32 v3, vcc, 0, v1, vcc
	v_add_co_u32_e32 v4, vcc, s25, v0
	v_mov_b32_e32 v66, 0
	s_nop 0
	v_addc_co_u32_e32 v5, vcc, 0, v1, vcc
	v_add_co_u32_e32 v6, vcc, s26, v0
	v_mov_b32_e32 v67, 0
	s_nop 0
	v_addc_co_u32_e32 v7, vcc, 0, v1, vcc
	v_add_co_u32_e32 v8, vcc, s27, v0
	s_nop 1
	v_addc_co_u32_e32 v9, vcc, 0, v1, vcc
	v_add_co_u32_e32 v10, vcc, s28, v0
	s_nop 1
	v_addc_co_u32_e32 v11, vcc, 0, v1, vcc
	v_add_co_u32_e32 v12, vcc, s29, v0
	s_nop 1
	v_addc_co_u32_e32 v13, vcc, 0, v1, vcc
	global_load_dword v59, v[6:7], off offset:-4096
	global_load_dword v51, v[6:7], off
	global_load_dword v50, v[8:9], off offset:-4096
	global_load_dword v44, v[8:9], off
	global_load_dword v48, v[10:11], off offset:-4096
	global_load_dword v43, v[10:11], off
	global_load_dword v45, v[12:13], off offset:-4096
	global_load_dword v27, v[12:13], off
	v_add_co_u32_e32 v6, vcc, 0xd000, v0
	s_nop 1
	v_addc_co_u32_e32 v7, vcc, 0, v1, vcc
	v_add_co_u32_e32 v8, vcc, 0xe000, v0
	s_nop 1
	v_addc_co_u32_e32 v9, vcc, 0, v1, vcc
	v_add_co_u32_e32 v10, vcc, 0xf000, v0
	s_nop 1
	v_addc_co_u32_e32 v11, vcc, 0, v1, vcc
	global_load_dword v65, v[0:1], off
	global_load_dword v63, v[2:3], off offset:-4096
	global_load_dword v62, v[2:3], off
	global_load_dword v61, v[4:5], off offset:-4096
	global_load_dword v60, v[4:5], off
	global_load_dword v52, v[6:7], off
	global_load_dword v46, v[8:9], off
	global_load_dword v47, v[10:11], off
	s_and_saveexec_b64 s[20:21], s[4:5]
	s_cbranch_execz .LBB0_1031
	v_lshl_add_u64 v[0:1], s[10:11], 0, v[22:23]
	v_lshl_add_u64 v[0:1], v[0:1], 4, s[16:17]
	global_load_dwordx4 v[0:3], v[0:1], off
	s_waitcnt vmcnt(0)
	v_xor_b32_e32 v4, v0, v1
	v_xor_b32_e32 v6, v2, v3
	v_ffbh_i32_e32 v5, v1
	v_ffbh_i32_e32 v7, v3
	v_ashrrev_i32_e32 v4, 31, v4
	v_ashrrev_i32_e32 v6, 31, v6
	v_add_u32_e32 v5, -1, v5
	v_add_u32_e32 v7, -1, v7
	v_add_u32_e32 v4, 32, v4
	v_add_u32_e32 v6, 32, v6
	v_min_u32_e32 v4, v5, v4
	v_min_u32_e32 v5, v7, v6
	v_lshlrev_b64 v[0:1], v4, v[0:1]
	v_lshlrev_b64 v[2:3], v5, v[2:3]
	v_min_u32_e32 v0, 1, v0
	v_min_u32_e32 v2, 1, v2
	v_or_b32_e32 v0, v1, v0
	v_or_b32_e32 v1, v3, v2
	v_cvt_f32_i32_e32 v0, v0
	v_cvt_f32_i32_e32 v1, v1
	v_sub_u32_e32 v2, 32, v4
	v_sub_u32_e32 v3, 32, v5
	v_ldexp_f32 v0, v0, v2
	v_ldexp_f32 v1, v1, v3
	v_mul_f32_e32 v66, 0x33800000, v0
	v_mul_f32_e32 v67, 0x33800000, v1
	s_branch .LBB0_1031
